# phase-2 mLSTM state quad: all four chunks' K/V rows of a block requested at the block top (one exposed round trip per block instead of five); RG-LRU units rebalanced 6/3
# baseline (speedup 1.0000x reference)
; __device__ __forceinline__ int fresh_lane() { int l; asm volatile("v_mbcnt_lo_u32_b32 %0, -1, 0\n\tv_mbcnt_hi_u32_b32 %0, -1, %0" : "=v"(l)); __builtin_assume(l >= 0 && l < 64); return l; }
; __device__ __forceinline__ float logsigmoidf_(float x) { return fminf(x, 0.f) - log1pf(__expf(-fabsf(x))); }
; __device__ __forceinline__ void ml_gates(const Args& a, unsigned char* lds_g, int rowbase, int h, int tid) {
;     const int lane = fresh_lane(), w = __builtin_amdgcn_readfirstlane(tid >> 6), dir = w >> 2, c = w & 3;
;     const float* GT = (const float*)(a.ws + WS_GATES) + (size_t)(rowbase + 64 * c + lane) * 32;
;     const float ipre = GT[(dir * 2) * 8 + h], fpre = GT[(dir * 2 + 1) * 8 + h];
;     float bsum = logsigmoidf_(fpre);
;     if (dir == 0) {
; #pragma unroll
;         for (int o = 1; o < 64; o <<= 1) { const float t = __shfl_up(bsum, o); if (lane >= o) bsum += t; }
; template <bool OUT, bool PASS2>
; __device__ __forceinline__ void ml_block(const Args& a, unsigned char* lds_g, int rowbase, int h, int dir, f32x4 (&st)[9], int tid) {
;     ...
;     ML_LOADC(dir ? 3 : 0);
.LBB0_266:
	s_add_i32 s6, s30, s49
	s_add_i32 s7, s6, 4
	s_and_b64 s[0:1], s[16:17], exec
	s_cselect_b32 s0, s29, s7
	s_lshl_b32 s0, s0, 8
	s_add_i32 s0, s31, s0
	s_cmp_eq_u32 s6, 4
	s_cselect_b32 s50, s33, s0
	v_readfirstlane_b32 s0, v180
	s_bfe_u32 s54, s0, 0x20006
	s_lshl_b32 s1, s54, 6
	v_mbcnt_lo_u32_b32 v0, -1, 0
	v_mbcnt_hi_u32_b32 v0, -1, v0
	s_lshr_b32 s51, s0, 8
	v_or_b32_e32 v2, s1, v0
	v_or_b32_e32 v2, s50, v2
	v_ashrrev_i32_e32 v3, 31, v2
	v_lshlrev_b64 v[2:3], 7, v[2:3]
	s_lshl_b32 s6, s51, 6
	v_lshl_add_u64 v[2:3], s[10:11], 0, v[2:3]
	s_or_b32 s14, s6, s48
	v_lshl_add_u64 v[2:3], v[2:3], 0, s[14:15]
	global_load_dword v50, v[2:3], off offset:32
	s_nop 0
	global_load_dword v2, v[2:3], off
	v_or_b32_e32 v181, s50, v51
	v_mov_b32_e32 v183, 0
	v_or_b32_e32 v182, s35, v181
	v_lshlrev_b32_e32 v182, 11, v182
	v_lshl_add_u64 v[120:121], v[46:47], 0, v[182:183]
	v_lshl_add_u64 v[122:123], v[48:49], 0, v[182:183]
	global_load_dwordx4 v[184:187], v[120:121], off offset:16
	global_load_dwordx4 v[188:191], v[120:121], off
	global_load_dwordx4 v[192:195], v[122:123], off
	global_load_dwordx4 v[196:199], v[122:123], off offset:16
	v_or_b32_e32 v182, s37, v181
	v_lshlrev_b32_e32 v182, 11, v182
	v_lshl_add_u64 v[124:125], v[46:47], 0, v[182:183]
	v_lshl_add_u64 v[126:127], v[48:49], 0, v[182:183]
	global_load_dwordx4 v[200:203], v[124:125], off offset:16
	global_load_dwordx4 v[204:207], v[124:125], off
	global_load_dwordx4 v[208:211], v[126:127], off
	global_load_dwordx4 v[212:215], v[126:127], off offset:16
	v_or_b32_e32 v182, s40, v181
	v_lshlrev_b32_e32 v182, 11, v182
	v_lshl_add_u64 v[128:129], v[46:47], 0, v[182:183]
	v_lshl_add_u64 v[130:131], v[48:49], 0, v[182:183]
	global_load_dwordx4 v[216:219], v[128:129], off offset:16
	global_load_dwordx4 v[220:223], v[128:129], off
	global_load_dwordx4 v[224:227], v[130:131], off
	global_load_dwordx4 v[228:231], v[130:131], off offset:16
	v_or_b32_e32 v182, s43, v181
	v_lshlrev_b32_e32 v182, 11, v182
	v_lshl_add_u64 v[132:133], v[46:47], 0, v[182:183]
	v_lshl_add_u64 v[134:135], v[48:49], 0, v[182:183]
	global_load_dwordx4 v[232:235], v[132:133], off offset:16
	global_load_dwordx4 v[236:239], v[132:133], off
	global_load_dwordx4 v[240:243], v[134:135], off
	global_load_dwordx4 v[244:247], v[134:135], off offset:16
	s_mov_b64 s[6:7], -1
	s_cmpk_lt_u32 s0, 0x100
	s_waitcnt vmcnt(16)
	v_mul_f32_e64 v3, |v50|, s23
	v_exp_f32_e32 v3, v3
	v_max_f32_e32 v50, v50, v50
	v_min_f32_e32 v50, 0, v50
	v_add_f32_e32 v72, 1.0, v3
	v_add_f32_e32 v73, -1.0, v72
	v_frexp_mant_f32_e32 v78, v72
	v_cvt_f64_f32_e32 v[70:71], v72
	v_sub_f32_e32 v79, v73, v72
	v_frexp_exp_i32_f64_e32 v70, v[70:71]
	v_cmp_gt_f32_e32 vcc, s24, v78
	v_sub_f32_e32 v73, v3, v73
	v_add_f32_e32 v71, 1.0, v79
	v_subbrev_co_u32_e32 v70, vcc, 0, v70, vcc
	v_add_f32_e32 v71, v73, v71
	v_sub_u32_e32 v73, 0, v70
	v_cvt_f32_i32_e32 v70, v70
	v_ldexp_f32 v72, v72, v73
	v_ldexp_f32 v71, v71, v73
	v_add_f32_e32 v73, -1.0, v72
	v_add_f32_e32 v78, 1.0, v72
	v_add_f32_e32 v79, 1.0, v73
	v_add_f32_e32 v80, -1.0, v78
	v_sub_f32_e32 v79, v72, v79
	v_sub_f32_e32 v72, v72, v80
	v_mul_f32_e32 v80, 0x3f317218, v70
	v_add_f32_e32 v79, v71, v79
	v_add_f32_e32 v71, v71, v72
	v_fma_f32 v72, v70, s25, -v80
	v_add_f32_e32 v81, v73, v79
	v_add_f32_e32 v82, v78, v71
	v_fmac_f32_e32 v72, 0xb102e308, v70
	v_sub_f32_e32 v70, v81, v73
	v_sub_f32_e32 v73, v82, v78
	v_rcp_f32_e32 v78, v82
	v_add_f32_e32 v83, v80, v72
	v_sub_f32_e32 v71, v71, v73
	v_sub_f32_e32 v73, v83, v80
	v_sub_f32_e32 v72, v72, v73
	v_mul_f32_e32 v73, v81, v78
	v_sub_f32_e32 v70, v79, v70
	v_mul_f32_e32 v79, v82, v73
	v_fma_f32 v80, v73, v82, -v79
	v_fmac_f32_e32 v80, v73, v71
	v_add_f32_e32 v84, v79, v80
	v_sub_f32_e32 v85, v81, v84
	v_sub_f32_e32 v79, v84, v79
	v_sub_f32_e32 v81, v81, v85
	v_sub_f32_e32 v79, v79, v80
	v_sub_f32_e32 v80, v81, v84
	v_add_f32_e32 v70, v70, v80
	v_add_f32_e32 v70, v79, v70
	v_add_f32_e32 v79, v85, v70
	v_mul_f32_e32 v80, v78, v79
	v_sub_f32_e32 v81, v85, v79
	v_mul_f32_e32 v84, v82, v80
	v_add_f32_e32 v70, v70, v81
	v_add_f32_e32 v81, v73, v80
	v_fma_f32 v82, v80, v82, -v84
	v_sub_f32_e32 v73, v81, v73
	v_fmac_f32_e32 v82, v80, v71
	v_sub_f32_e32 v71, v80, v73
	v_add_f32_e32 v73, v84, v82
	v_sub_f32_e32 v80, v73, v84
	v_sub_f32_e32 v84, v79, v73
	v_sub_f32_e32 v79, v79, v84
	v_sub_f32_e32 v73, v79, v73
	v_sub_f32_e32 v80, v80, v82
	v_add_f32_e32 v70, v70, v73
	v_add_f32_e32 v70, v80, v70
	v_add_f32_e32 v70, v84, v70
	v_mul_f32_e32 v70, v78, v70
	v_add_f32_e32 v70, v71, v70
	v_add_f32_e32 v71, v81, v70
	v_mul_f32_e32 v73, v71, v71
	v_fmamk_f32 v80, v73, 0x3e9b6dac, v60
	v_sub_f32_e32 v78, v71, v81
	v_ldexp_f32 v79, v71, 1
	v_mul_f32_e32 v71, v71, v73
	v_fmaak_f32 v73, v73, v80, 0x3f2aaada
	v_mul_f32_e32 v71, v71, v73
	v_add_f32_e32 v73, v79, v71
	v_sub_f32_e32 v70, v70, v78
	v_sub_f32_e32 v78, v73, v79
	v_ldexp_f32 v70, v70, 1
	v_sub_f32_e32 v71, v71, v78
	v_add_f32_e32 v70, v70, v71
	v_add_f32_e32 v71, v73, v70
	v_sub_f32_e32 v73, v71, v73
	v_add_f32_e32 v78, v83, v71
	v_sub_f32_e32 v70, v70, v73
	v_sub_f32_e32 v73, v78, v83
	v_sub_f32_e32 v79, v78, v73
	v_sub_f32_e32 v71, v71, v73
	v_add_f32_e32 v73, v72, v70
	v_sub_f32_e32 v79, v83, v79
	v_sub_f32_e32 v80, v73, v72
	v_add_f32_e32 v71, v71, v79
	v_sub_f32_e32 v79, v73, v80
	v_sub_f32_e32 v70, v70, v80
	v_sub_f32_e32 v72, v72, v79
	v_add_f32_e32 v71, v73, v71
	v_add_f32_e32 v70, v70, v72
	v_add_f32_e32 v72, v78, v71
	v_sub_f32_e32 v73, v72, v78
	v_sub_f32_e32 v71, v71, v73
	v_add_f32_e32 v70, v70, v71
	v_add_f32_e32 v70, v72, v70
	v_cmp_neq_f32_e32 vcc, s26, v3
	s_nop 1
	v_cndmask_b32_e32 v70, v61, v70, vcc
	v_cmp_ngt_f32_e32 vcc, -1.0, v3
	s_nop 1
	v_cndmask_b32_e32 v70, v62, v70, vcc
	v_cmp_neq_f32_e32 vcc, -1.0, v3
	s_nop 1
	v_cndmask_b32_e32 v70, v63, v70, vcc
	v_cmp_lt_f32_e64 vcc, |v3|, s27
	s_nop 1
	v_cndmask_b32_e32 v3, v70, v3, vcc
	v_sub_f32_e32 v3, v50, v3
	v_cmp_gt_u32_e32 vcc, 32, v0
	s_cbranch_scc1 .LBB0_268
; __device__ __forceinline__ void ml_gates(const Args& a, unsigned char* lds_g, int rowbase, int h, int tid) {
;     ...
;     } else {
; #pragma unroll
;         for (int o = 1; o < 64; o <<= 1) { const float t = __shfl_down(bsum, o); if (lane + o < 64) bsum += t; }
;     }
	v_and_b32_e32 v50, 63, v64
	v_cmp_ne_u32_e64 s[6:7], 63, v50
	s_nop 1
	v_addc_co_u32_e64 v70, s[6:7], 0, v64, s[6:7]
	v_lshlrev_b32_e32 v70, 2, v70
	ds_bpermute_b32 v70, v70, v3
	v_cmp_eq_u32_e64 s[6:7], 63, v0
	s_waitcnt lgkmcnt(0)
	v_add_f32_e32 v70, v3, v70
	v_cndmask_b32_e64 v70, v70, v3, s[6:7]
	v_cmp_gt_u32_e64 s[6:7], 62, v50
	s_nop 1
	v_cndmask_b32_e64 v71, 0, 2, s[6:7]
	v_add_lshl_u32 v71, v71, v64, 2
	ds_bpermute_b32 v71, v71, v70
	v_cmp_gt_u32_e64 s[6:7], 62, v0
	s_waitcnt lgkmcnt(0)
	v_add_f32_e32 v71, v70, v71
	v_cndmask_b32_e64 v70, v70, v71, s[6:7]
	v_cmp_gt_u32_e64 s[6:7], 60, v50
	s_nop 1
	v_cndmask_b32_e64 v71, 0, 4, s[6:7]
	v_add_lshl_u32 v71, v71, v64, 2
	ds_bpermute_b32 v71, v71, v70
	v_cmp_gt_u32_e64 s[6:7], 60, v0
	s_waitcnt lgkmcnt(0)
	v_add_f32_e32 v71, v70, v71
	v_cndmask_b32_e64 v70, v70, v71, s[6:7]
	v_cmp_gt_u32_e64 s[6:7], 56, v50
	s_nop 1
	v_cndmask_b32_e64 v71, 0, 8, s[6:7]
	v_add_lshl_u32 v71, v71, v64, 2
	ds_bpermute_b32 v71, v71, v70
	v_cmp_gt_u32_e64 s[6:7], 56, v0
	s_waitcnt lgkmcnt(0)
	v_add_f32_e32 v71, v70, v71
	v_cndmask_b32_e64 v70, v70, v71, s[6:7]
	v_cmp_gt_u32_e64 s[6:7], 48, v50
	s_nop 1
	v_cndmask_b32_e64 v50, 0, 16, s[6:7]
	v_add_lshl_u32 v50, v50, v64, 2
	ds_bpermute_b32 v50, v50, v70
	v_cmp_gt_u32_e64 s[6:7], 48, v0
	s_waitcnt lgkmcnt(0)
	v_add_f32_e32 v50, v70, v50
	v_cndmask_b32_e64 v50, v70, v50, s[6:7]
	ds_bpermute_b32 v70, v65, v50
	s_mov_b64 s[6:7], 0
	s_waitcnt lgkmcnt(0)
	v_add_f32_e32 v70, v50, v70
	v_cndmask_b32_e32 v50, v50, v70, vcc

; #define WG_BAR() do { asm volatile("s_waitcnt lgkmcnt(0)" ::: "memory"); __builtin_amdgcn_s_barrier(); asm volatile("" ::: "memory"); } while (0)
; __device__ __forceinline__ unsigned f2bf(float f) { unsigned u = __builtin_bit_cast(unsigned, f); return (u + 0x7fffu + ((u >> 16) & 1u)) >> 16; }
; __device__ __forceinline__ unsigned pk2(float lo, float hi) { return pg8::cvt_pk_bf16(lo, hi); }
; template <bool OUT, bool PASS2>
; __device__ __forceinline__ void ml_block(const Args& a, unsigned char* lds_g, int rowbase, int h, int dir, f32x4 (&st)[9], int tid) {
;     ...
;         {
;             const int t = st_t, pc = st_pc;
;             const float e = eu[64 * c + t];
;             *(v4u*)(Ki + t * ML_STRIDE + 16 * pc) = k0; *(v4u*)(Ki + t * ML_STRIDE + 16 * pc + 8) = k1;
;             if (OUT) { *(v4u*)(Qi + t * ML_STRIDE + 16 * pc) = q0; *(v4u*)(Qi + t * ML_STRIDE + 16 * pc + 8) = q1; }
;             const unsigned vv[8] = {v0.x, v0.y, v0.z, v0.w, v1.x, v1.y, v1.z, v1.w}; unsigned o[8];
; #pragma unroll
;             for (int i = 0; i < 8; ++i) o[i] = pk2(bflo(vv[i]) * e, bfhi(vv[i]) * e);
;             *(v4u*)(Vi + t * ML_STRIDE + 16 * pc) = (v4u){o[0], o[1], o[2], o[3]}; *(v4u*)(Vi + t * ML_STRIDE + 16 * pc + 8) = (v4u){o[4], o[5], o[6], o[7]};
;             if (pc == 0) { *(v4u*)(AUGi + t * 16) = (v4u){f2bf(e), 0u, 0u, 0u}; *(v4u*)(AUGi + t * 16 + 8) = (v4u){0u, 0u, 0u, 0u}; }
;         }
;         WG_BAR();
;         if (ci < 3) ML_LOADC(dir ? 2 - ci : ci + 1);
;     ...
;             for (int ks = 0; ks < 2; ++ks) { const bf16x8_t kf = frag_tr(Ki, ML_STRIDE, 32 * ks, 16 * w, lane);
; #pragma unroll
;                 for (int vt = 0; vt < 8; ++vt) st[vt] = __builtin_amdgcn_mfma_f32_16x16x32_bf16(kf, frag_tr(Vi, ML_STRIDE, 32 * ks, 16 * vt, lane), st[vt], 0, 0, 0);
;                 st[8] = __builtin_amdgcn_mfma_f32_16x16x32_bf16(kf, frag_tr(AUGi, 16, 32 * ks, 0, lane), st[8], 0, 0, 0); }
.LBB0_272:
	s_or_b64 exec, exec, s[0:1]
	v_or_b32_e32 v73, s50, v51
	s_waitcnt lgkmcnt(2)
	v_or_b32_e32 v2, s35, v73
	v_ashrrev_i32_e32 v3, 31, v2
	v_lshlrev_b64 v[2:3], 11, v[2:3]
	s_waitcnt lgkmcnt(0)
	s_barrier
	v_lshl_add_u64 v[70:71], v[46:47], 0, v[2:3]
	v_lshl_add_u64 v[2:3], v[48:49], 0, v[2:3]
	v_add_u32_e32 v0, s36, v69
	ds_read_b32 v0, v0
	v_readfirstlane_b32 s6, v180
	s_waitcnt vmcnt(12)
	v_mov_b64_e32 v[78:79], v[184:185]
	v_mov_b64_e32 v[80:81], v[186:187]
	v_mov_b64_e32 v[82:83], v[188:189]
	v_mov_b64_e32 v[84:85], v[190:191]
	v_mov_b64_e32 v[86:87], v[192:193]
	v_mov_b64_e32 v[88:89], v[194:195]
	v_mov_b64_e32 v[90:91], v[196:197]
	v_mov_b64_e32 v[92:93], v[198:199]
	ds_write_b128 v53, v[82:85] offset:17408
	ds_write_b128 v53, v[78:81] offset:17424
	v_lshlrev_b32_e32 v2, 16, v86
	v_and_b32_e32 v3, 0xffff0000, v86
	v_lshlrev_b32_e32 v70, 16, v87
	v_and_b32_e32 v71, 0xffff0000, v87
	v_lshlrev_b32_e32 v78, 16, v88
	v_and_b32_e32 v79, 0xffff0000, v88
	v_lshlrev_b32_e32 v80, 16, v89
	v_and_b32_e32 v81, 0xffff0000, v89
	v_lshlrev_b32_e32 v82, 16, v90
	v_and_b32_e32 v83, 0xffff0000, v90
	v_lshlrev_b32_e32 v84, 16, v91
	v_and_b32_e32 v85, 0xffff0000, v91
	v_lshlrev_b32_e32 v86, 16, v92
	v_and_b32_e32 v87, 0xffff0000, v92
	v_lshlrev_b32_e32 v88, 16, v93
	v_and_b32_e32 v89, 0xffff0000, v93
	s_waitcnt lgkmcnt(2)
	v_pk_mul_f32 v[2:3], v[0:1], v[2:3] op_sel_hi:[0,1]
	v_pk_mul_f32 v[70:71], v[0:1], v[70:71] op_sel_hi:[0,1]
	v_pk_mul_f32 v[90:91], v[0:1], v[78:79] op_sel_hi:[0,1]
	v_pk_mul_f32 v[92:93], v[0:1], v[80:81] op_sel_hi:[0,1]
	v_pk_mul_f32 v[82:83], v[0:1], v[82:83] op_sel_hi:[0,1]
	v_pk_mul_f32 v[84:85], v[0:1], v[84:85] op_sel_hi:[0,1]
	v_pk_mul_f32 v[86:87], v[0:1], v[86:87] op_sel_hi:[0,1]
	v_pk_mul_f32 v[88:89], v[0:1], v[88:89] op_sel_hi:[0,1]
	v_cvt_pk_bf16_f32 v78, v2, v3
	v_cvt_pk_bf16_f32 v79, v70, v71
	v_cvt_pk_bf16_f32 v80, v90, v91
	v_cvt_pk_bf16_f32 v81, v92, v93
	v_cvt_pk_bf16_f32 v82, v82, v83
	v_cvt_pk_bf16_f32 v83, v84, v85
	v_cvt_pk_bf16_f32 v84, v86, v87
	v_cvt_pk_bf16_f32 v85, v88, v89
	ds_write_b128 v53, v[78:81] offset:34816
	ds_write_b128 v53, v[82:85] offset:34832
	s_and_saveexec_b64 s[0:1], s[8:9]
	s_cbranch_execz .LBB0_274
	v_bfe_u32 v2, v0, 16, 1
	v_add3_u32 v0, v0, v2, s28
	v_lshrrev_b32_e32 v0, 16, v0
	v_mov_b32_e32 v2, v1
	v_mov_b32_e32 v3, v1
	ds_write_b128 v66, v[0:3] offset:52224
	ds_write_b128 v66, v[74:77] offset:52240
.LBB0_274:
	s_or_b64 exec, exec, s[0:1]
	s_lshr_b32 s0, s6, 1
	s_and_b32 s0, s0, 0x7fffffe0
	v_add_u32_e32 v0, s0, v54
	s_waitcnt lgkmcnt(0)
	s_barrier
	v_lshl_add_u32 v71, v55, 1, v0
	ds_read_b64_tr_b16 v[78:79], v71 offset:17408
	ds_read_b64_tr_b16 v[80:81], v71 offset:18496
	ds_read_b64_tr_b16 v[82:83], v56 offset:34816
	ds_read_b64_tr_b16 v[86:87], v56 offset:34848
	ds_read_b64_tr_b16 v[90:91], v56 offset:34880
	ds_read_b64_tr_b16 v[94:95], v56 offset:34912
	ds_read_b64_tr_b16 v[84:85], v56 offset:35904
	ds_read_b64_tr_b16 v[88:89], v56 offset:35936
	ds_read_b64_tr_b16 v[92:93], v56 offset:35968
	ds_read_b64_tr_b16 v[96:97], v56 offset:36000
	v_lshl_add_u32 v72, v58, 1, v0
	ds_read_b64_tr_b16 v[98:99], v72 offset:17408
	ds_read_b64_tr_b16 v[100:101], v72 offset:18496
	s_waitcnt lgkmcnt(5)
	v_mfma_f32_16x16x32_bf16 v[36:39], v[78:81], v[82:85], v[36:39]
	v_add_u32_e32 v70, v54, v57
	v_mov_b32_e32 v0, s38
	s_waitcnt lgkmcnt(4)
	v_mfma_f32_16x16x32_bf16 v[32:35], v[78:81], v[86:89], v[32:35]
	s_waitcnt lgkmcnt(3)
	v_mfma_f32_16x16x32_bf16 v[28:31], v[78:81], v[90:93], v[28:31]
	s_waitcnt lgkmcnt(2)
	v_mfma_f32_16x16x32_bf16 v[24:27], v[78:81], v[94:97], v[24:27]
	ds_read_b64_tr_b16 v[84:85], v56 offset:36032
	ds_read_b64_tr_b16 v[82:83], v56 offset:34944
	ds_read_b64_tr_b16 v[86:87], v56 offset:34976
	ds_read_b64_tr_b16 v[90:91], v56 offset:35008
	ds_read_b64_tr_b16 v[94:95], v56 offset:35040
	ds_read_b64_tr_b16 v[88:89], v56 offset:36064
	ds_read_b64_tr_b16 v[92:93], v56 offset:36096
	ds_read_b64_tr_b16 v[96:97], v56 offset:36128
	s_waitcnt lgkmcnt(6)
	v_mfma_f32_16x16x32_bf16 v[20:23], v[78:81], v[82:85], v[20:23]
	s_waitcnt lgkmcnt(2)
	v_mfma_f32_16x16x32_bf16 v[82:85], v[78:81], v[86:89], v[16:19]
	s_waitcnt lgkmcnt(1)
	v_mfma_f32_16x16x32_bf16 v[86:89], v[78:81], v[90:93], v[12:15]
	s_waitcnt lgkmcnt(0)
	v_mfma_f32_16x16x32_bf16 v[90:93], v[78:81], v[94:97], v[8:11]
	s_nop 2
	ds_read_b64_tr_b16 v[8:9], v70 offset:52224
	ds_read_b64_tr_b16 v[10:11], v70 offset:52352
	ds_read_b64_tr_b16 v[94:95], v67 offset:52224
	ds_read_b64_tr_b16 v[96:97], v67 offset:52352
	s_waitcnt lgkmcnt(2)
	v_mfma_f32_16x16x32_bf16 v[78:81], v[78:81], v[8:11], v[4:7]
	s_nop 2
	ds_read_b64_tr_b16 v[4:5], v59 offset:35904
	ds_read_b64_tr_b16 v[2:3], v59 offset:34816
	ds_read_b64_tr_b16 v[6:7], v59 offset:34848
	ds_read_b64_tr_b16 v[12:13], v59 offset:34880
	ds_read_b64_tr_b16 v[16:17], v59 offset:34912
	ds_read_b64_tr_b16 v[8:9], v59 offset:35936
	ds_read_b64_tr_b16 v[14:15], v59 offset:35968
	ds_read_b64_tr_b16 v[18:19], v59 offset:36000
	s_waitcnt lgkmcnt(6)
	v_mfma_f32_16x16x32_bf16 v[36:39], v[98:101], v[2:5], v[36:39]
	v_or_b32_e32 v2, s37, v73
	v_ashrrev_i32_e32 v3, 31, v2
	v_lshlrev_b64 v[2:3], 11, v[2:3]
	v_lshl_add_u64 v[118:119], v[48:49], 0, v[2:3]
	v_lshl_add_u64 v[2:3], v[46:47], 0, v[2:3]
	s_waitcnt lgkmcnt(2)
	v_mfma_f32_16x16x32_bf16 v[8:11], v[98:101], v[6:9], v[32:35]
	s_waitcnt lgkmcnt(0)
	v_mfma_f32_16x16x32_bf16 v[16:19], v[98:101], v[16:19], v[24:27]
	ds_read_b64_tr_b16 v[4:5], v59 offset:36032
	ds_read_b64_tr_b16 v[2:3], v59 offset:34944
	s_nop 0
	ds_read_b64_tr_b16 v[24:25], v59 offset:34976
	ds_read_b64_tr_b16 v[32:33], v59 offset:35008
	ds_read_b64_tr_b16 v[110:111], v59 offset:35040
	ds_read_b64_tr_b16 v[26:27], v59 offset:36064
	ds_read_b64_tr_b16 v[34:35], v59 offset:36096
	ds_read_b64_tr_b16 v[112:113], v59 offset:36128
	ds_read_b32 v50, v0
	v_mfma_f32_16x16x32_bf16 v[12:15], v[98:101], v[12:15], v[28:31]
	s_waitcnt lgkmcnt(7)
	v_mfma_f32_16x16x32_bf16 v[28:31], v[98:101], v[2:5], v[20:23]
	v_add_u32_e32 v2, s39, v69
	s_waitcnt lgkmcnt(3)
	v_mfma_f32_16x16x32_bf16 v[4:7], v[98:101], v[24:27], v[82:85]
	s_nop 2
	s_waitcnt lgkmcnt(0)
	s_barrier
; template <bool OUT, bool PASS2>
; __device__ __forceinline__ void ml_block(const Args& a, unsigned char* lds_g, int rowbase, int h, int dir, f32x4 (&st)[9], int tid) {
;     ...
;         {
;             const int t = st_t, pc = st_pc;
;             const float e = eu[64 * c + t];
;             *(v4u*)(Ki + t * ML_STRIDE + 16 * pc) = k0; *(v4u*)(Ki + t * ML_STRIDE + 16 * pc + 8) = k1;
;             if (OUT) { *(v4u*)(Qi + t * ML_STRIDE + 16 * pc) = q0; *(v4u*)(Qi + t * ML_STRIDE + 16 * pc + 8) = q1; }
;             const unsigned vv[8] = {v0.x, v0.y, v0.z, v0.w, v1.x, v1.y, v1.z, v1.w}; unsigned o[8];
; #pragma unroll
;             for (int i = 0; i < 8; ++i) o[i] = pk2(bflo(vv[i]) * e, bfhi(vv[i]) * e);
;             *(v4u*)(Vi + t * ML_STRIDE + 16 * pc) = (v4u){o[0], o[1], o[2], o[3]}; *(v4u*)(Vi + t * ML_STRIDE + 16 * pc + 8) = (v4u){o[4], o[5], o[6], o[7]};
;             if (pc == 0) { *(v4u*)(AUGi + t * 16) = (v4u){f2bf(e), 0u, 0u, 0u}; *(v4u*)(AUGi + t * 16 + 8) = (v4u){0u, 0u, 0u, 0u}; }
;         }
;         WG_BAR();
;         if (ci < 3) ML_LOADC(dir ? 2 - ci : ci + 1);
;         f32x4 X[5]; float hval[4][4];
;         if (OUT) {
;             bf16x8_t qf[4];
; #pragma unroll
;             for (int ks = 0; ks < 4; ++ks) qf[ks] = frag_row(Qi, 16 * ti, 32 * ks, fr, fq);
;             bf16x8_t P[2]; bool pv[2];
; #pragma unroll
;             for (int pp = 0; pp < 2; ++pp) {
;                 f32x4 d[2];
; #pragma unroll
;                 for (int hh = 0; hh < 2; ++hh) { const int si = 2 * pp + hh; d[hh] = (f32x4){0.f, 0.f, 0.f, 0.f};
;                     const bool valid = dir ? (si >= ti) : (si <= ti);
;                     if (valid) {
; #pragma unroll
;                         for (int ks = 0; ks < 4; ++ks) d[hh] = __builtin_amdgcn_mfma_f32_16x16x32_bf16(frag_row(Ki, 16 * si, 32 * ks, fr, fq), qf[ks], d[hh], 0, 0, 0);
;                         if (si == ti) {
; #pragma unroll
;                             for (int r = 0; r < 4; ++r) { const bool keep = dir ? (4 * fq + r >= fr) : (4 * fq + r <= fr); d[hh][r] = keep ? d[hh][r] : 0.f; } } } }
;                 pv[pp] = dir ? (2 * pp + 1 >= ti) : (2 * pp <= ti);
;                 const unsigned p0 = pk2(d[0][0], d[0][1]), p1 = pk2(d[0][2], d[0][3]), p2 = pk2(d[1][0], d[1][1]), p3 = pk2(d[1][2], d[1][3]);
;                 P[pp] = __builtin_bit_cast(bf16x8_t, (v4u){p0, p1, p2, p3});
;             }
	ds_read_b32 v0, v2
	v_mfma_f32_16x16x32_bf16 v[24:27], v[98:101], v[94:97], v[78:81]
	s_waitcnt vmcnt(8)
	v_mov_b64_e32 v[102:103], v[200:201]
	v_mov_b64_e32 v[104:105], v[202:203]
	v_mov_b64_e32 v[106:107], v[204:205]
	v_mov_b64_e32 v[108:109], v[206:207]
	v_mov_b64_e32 v[114:115], v[208:209]
	v_mov_b64_e32 v[116:117], v[210:211]
	v_mov_b64_e32 v[82:83], v[212:213]
	v_mov_b64_e32 v[84:85], v[214:215]
	ds_write_b128 v53, v[106:109] offset:17408
	ds_write_b128 v53, v[102:105] offset:17424
	s_waitcnt lgkmcnt(5)
	v_mfma_f32_16x16x32_bf16 v[20:23], v[98:101], v[32:35], v[86:89]
	v_lshlrev_b32_e32 v2, 16, v114
	v_and_b32_e32 v3, 0xffff0000, v114
	s_waitcnt lgkmcnt(2)
	v_pk_mul_f32 v[2:3], v[0:1], v[2:3] op_sel_hi:[0,1]
	v_cvt_pk_bf16_f32 v78, v2, v3
	v_lshlrev_b32_e32 v2, 16, v115
	v_and_b32_e32 v3, 0xffff0000, v115
	v_pk_mul_f32 v[2:3], v[0:1], v[2:3] op_sel_hi:[0,1]
	v_cvt_pk_bf16_f32 v79, v2, v3
	v_lshlrev_b32_e32 v2, 16, v116
	v_and_b32_e32 v3, 0xffff0000, v116
	v_pk_mul_f32 v[2:3], v[0:1], v[2:3] op_sel_hi:[0,1]
	v_cvt_pk_bf16_f32 v80, v2, v3
	v_lshlrev_b32_e32 v2, 16, v117
	v_and_b32_e32 v3, 0xffff0000, v117
	v_pk_mul_f32 v[2:3], v[0:1], v[2:3] op_sel_hi:[0,1]
	v_cvt_pk_bf16_f32 v81, v2, v3
	v_lshlrev_b32_e32 v2, 16, v82
	v_and_b32_e32 v3, 0xffff0000, v82
	v_pk_mul_f32 v[2:3], v[0:1], v[2:3] op_sel_hi:[0,1]
	v_cvt_pk_bf16_f32 v82, v2, v3
	v_lshlrev_b32_e32 v2, 16, v83
	v_and_b32_e32 v3, 0xffff0000, v83
	v_pk_mul_f32 v[2:3], v[0:1], v[2:3] op_sel_hi:[0,1]
	v_mfma_f32_16x16x32_bf16 v[32:35], v[98:101], v[110:113], v[90:93]
	v_cvt_pk_bf16_f32 v83, v2, v3
	v_lshlrev_b32_e32 v2, 16, v84
	v_and_b32_e32 v3, 0xffff0000, v84
	v_pk_mul_f32 v[2:3], v[0:1], v[2:3] op_sel_hi:[0,1]
	v_cvt_pk_bf16_f32 v84, v2, v3
	v_lshlrev_b32_e32 v2, 16, v85
	v_and_b32_e32 v3, 0xffff0000, v85
	v_pk_mul_f32 v[2:3], v[0:1], v[2:3] op_sel_hi:[0,1]
	v_cvt_pk_bf16_f32 v85, v2, v3
	ds_write_b128 v53, v[78:81] offset:34816
	ds_write_b128 v53, v[82:85] offset:34832
	s_and_saveexec_b64 s[0:1], s[8:9]
	s_cbranch_execz .LBB0_276
	v_bfe_u32 v2, v0, 16, 1
	v_add3_u32 v0, v0, v2, s28
	v_lshrrev_b32_e32 v0, 16, v0
	v_mov_b32_e32 v2, v1
	v_mov_b32_e32 v3, v1
	ds_write_b128 v66, v[0:3] offset:52224
	ds_write_b128 v66, v[74:77] offset:52240
.LBB0_276:
	s_or_b64 exec, exec, s[0:1]
	s_waitcnt lgkmcnt(0)
	s_barrier
	ds_read_b64_tr_b16 v[78:79], v71 offset:17408
	ds_read_b64_tr_b16 v[80:81], v71 offset:18496
	ds_read_b64_tr_b16 v[82:83], v56 offset:34816
	ds_read_b64_tr_b16 v[86:87], v56 offset:34848
	ds_read_b64_tr_b16 v[90:91], v56 offset:34880
	ds_read_b64_tr_b16 v[94:95], v56 offset:34912
	ds_read_b64_tr_b16 v[84:85], v56 offset:35904
	ds_read_b64_tr_b16 v[88:89], v56 offset:35936
	ds_read_b64_tr_b16 v[92:93], v56 offset:35968
	ds_read_b64_tr_b16 v[96:97], v56 offset:36000
	ds_read_b64_tr_b16 v[98:99], v72 offset:17408
	ds_read_b64_tr_b16 v[100:101], v72 offset:18496
	v_pk_mul_f32 v[38:39], v[38:39], v[50:51] op_sel_hi:[1,0]
	v_pk_mul_f32 v[36:37], v[36:37], v[50:51] op_sel_hi:[1,0]
	v_pk_mul_f32 v[10:11], v[10:11], v[50:51] op_sel_hi:[1,0]
	v_pk_mul_f32 v[8:9], v[8:9], v[50:51] op_sel_hi:[1,0]
	v_pk_mul_f32 v[14:15], v[14:15], v[50:51] op_sel_hi:[1,0]
	v_pk_mul_f32 v[12:13], v[12:13], v[50:51] op_sel_hi:[1,0]
	v_pk_mul_f32 v[18:19], v[18:19], v[50:51] op_sel_hi:[1,0]
	v_pk_mul_f32 v[16:17], v[16:17], v[50:51] op_sel_hi:[1,0]
	s_waitcnt lgkmcnt(5)
	v_mfma_f32_16x16x32_bf16 v[36:39], v[78:81], v[82:85], v[36:39]
	v_mul_f32_e64 v30, v30, v50
	v_mul_f32_e64 v31, v31, v50
	v_pk_mul_f32 v[28:29], v[28:29], v[50:51] op_sel_hi:[1,0]
	v_pk_mul_f32 v[6:7], v[6:7], v[50:51] op_sel_hi:[1,0]
	s_waitcnt lgkmcnt(4)
	v_mfma_f32_16x16x32_bf16 v[8:11], v[78:81], v[86:89], v[8:11]
	v_mul_f32_e64 v4, v4, v50
	v_mul_f32_e64 v5, v5, v50
	v_pk_mul_f32 v[22:23], v[22:23], v[50:51] op_sel_hi:[1,0]
	v_pk_mul_f32 v[20:21], v[20:21], v[50:51] op_sel_hi:[1,0]
	s_waitcnt lgkmcnt(3)
	v_mfma_f32_16x16x32_bf16 v[12:15], v[78:81], v[90:93], v[12:15]
	v_mul_f32_e64 v26, v26, v50
	v_mul_f32_e64 v27, v27, v50
	v_pk_mul_f32 v[24:25], v[24:25], v[50:51] op_sel_hi:[1,0]
	v_mov_b32_e32 v0, s41
	s_waitcnt lgkmcnt(2)
	v_mfma_f32_16x16x32_bf16 v[16:19], v[78:81], v[94:97], v[16:19]
	ds_read_b64_tr_b16 v[84:85], v56 offset:36032
	ds_read_b64_tr_b16 v[82:83], v56 offset:34944
	ds_read_b64_tr_b16 v[86:87], v56 offset:34976
	ds_read_b64_tr_b16 v[90:91], v56 offset:35008
	ds_read_b64_tr_b16 v[94:95], v56 offset:35040
	ds_read_b64_tr_b16 v[88:89], v56 offset:36064
	ds_read_b64_tr_b16 v[92:93], v56 offset:36096
	ds_read_b64_tr_b16 v[96:97], v56 offset:36128
	s_waitcnt lgkmcnt(6)
	v_mfma_f32_16x16x32_bf16 v[82:85], v[78:81], v[82:85], v[28:31]
	s_nop 2
	v_mul_f32_e64 v30, v34, v50
	v_mul_f32_e64 v31, v35, v50
	v_pk_mul_f32 v[28:29], v[32:33], v[50:51] op_sel_hi:[1,0]
	ds_read_b64_tr_b16 v[32:33], v70 offset:52224
	ds_read_b64_tr_b16 v[34:35], v70 offset:52352
	s_waitcnt lgkmcnt(4)
	v_mfma_f32_16x16x32_bf16 v[2:5], v[78:81], v[86:89], v[4:7]
	s_waitcnt lgkmcnt(3)
	v_mfma_f32_16x16x32_bf16 v[20:23], v[78:81], v[90:93], v[20:23]
	ds_read_b64_tr_b16 v[90:91], v67 offset:52224
	ds_read_b64_tr_b16 v[92:93], v67 offset:52352
	v_or_b32_e32 v6, s40, v73
	v_ashrrev_i32_e32 v7, 31, v6
	s_waitcnt lgkmcnt(4)
	v_mfma_f32_16x16x32_bf16 v[86:89], v[78:81], v[94:97], v[28:31]
	s_waitcnt lgkmcnt(2)
	v_mfma_f32_16x16x32_bf16 v[78:81], v[78:81], v[32:35], v[24:27]
	s_nop 2
	ds_read_b64_tr_b16 v[26:27], v59 offset:35904
	ds_read_b64_tr_b16 v[24:25], v59 offset:34816
	ds_read_b64_tr_b16 v[28:29], v59 offset:34848
	ds_read_b64_tr_b16 v[32:33], v59 offset:34880
	ds_read_b64_tr_b16 v[94:95], v59 offset:34912
	ds_read_b64_tr_b16 v[30:31], v59 offset:35936
	ds_read_b64_tr_b16 v[34:35], v59 offset:35968
	ds_read_b64_tr_b16 v[96:97], v59 offset:36000
	s_waitcnt lgkmcnt(6)
; template <bool OUT, bool PASS2>
; __device__ __forceinline__ void ml_block(const Args& a, unsigned char* lds_g, int rowbase, int h, int dir, f32x4 (&st)[9], int tid) {
;     ...
;         {
;             const int t = st_t, pc = st_pc;
;             const float e = eu[64 * c + t];
;             *(v4u*)(Ki + t * ML_STRIDE + 16 * pc) = k0; *(v4u*)(Ki + t * ML_STRIDE + 16 * pc + 8) = k1;
;             if (OUT) { *(v4u*)(Qi + t * ML_STRIDE + 16 * pc) = q0; *(v4u*)(Qi + t * ML_STRIDE + 16 * pc + 8) = q1; }
;             const unsigned vv[8] = {v0.x, v0.y, v0.z, v0.w, v1.x, v1.y, v1.z, v1.w}; unsigned o[8];
; #pragma unroll
;             for (int i = 0; i < 8; ++i) o[i] = pk2(bflo(vv[i]) * e, bfhi(vv[i]) * e);
;             *(v4u*)(Vi + t * ML_STRIDE + 16 * pc) = (v4u){o[0], o[1], o[2], o[3]}; *(v4u*)(Vi + t * ML_STRIDE + 16 * pc + 8) = (v4u){o[4], o[5], o[6], o[7]};
;             if (pc == 0) { *(v4u*)(AUGi + t * 16) = (v4u){f2bf(e), 0u, 0u, 0u}; *(v4u*)(AUGi + t * 16 + 8) = (v4u){0u, 0u, 0u, 0u}; }
;         }
;         WG_BAR();
;         if (ci < 3) ML_LOADC(dir ? 2 - ci : ci + 1);
;         f32x4 X[5]; float hval[4][4];
;         if (OUT) {
;             bf16x8_t qf[4];
; #pragma unroll
;             for (int ks = 0; ks < 4; ++ks) qf[ks] = frag_row(Qi, 16 * ti, 32 * ks, fr, fq);
;             bf16x8_t P[2]; bool pv[2];
; #pragma unroll
;             for (int pp = 0; pp < 2; ++pp) {
;                 f32x4 d[2];
; #pragma unroll
;                 for (int hh = 0; hh < 2; ++hh) { const int si = 2 * pp + hh; d[hh] = (f32x4){0.f, 0.f, 0.f, 0.f};
;                     const bool valid = dir ? (si >= ti) : (si <= ti);
;                     if (valid) {
; #pragma unroll
;                         for (int ks = 0; ks < 4; ++ks) d[hh] = __builtin_amdgcn_mfma_f32_16x16x32_bf16(frag_row(Ki, 16 * si, 32 * ks, fr, fq), qf[ks], d[hh], 0, 0, 0);
;                         if (si == ti) {
; #pragma unroll
;                             for (int r = 0; r < 4; ++r) { const bool keep = dir ? (4 * fq + r >= fr) : (4 * fq + r <= fr); d[hh][r] = keep ? d[hh][r] : 0.f; } } } }
;                 pv[pp] = dir ? (2 * pp + 1 >= ti) : (2 * pp <= ti);
;                 const unsigned p0 = pk2(d[0][0], d[0][1]), p1 = pk2(d[0][2], d[0][3]), p2 = pk2(d[1][0], d[1][1]), p3 = pk2(d[1][2], d[1][3]);
;                 P[pp] = __builtin_bit_cast(bf16x8_t, (v4u){p0, p1, p2, p3});
;             }
	v_mfma_f32_16x16x32_bf16 v[36:39], v[98:101], v[24:27], v[36:39]
	s_waitcnt lgkmcnt(2)
	v_mfma_f32_16x16x32_bf16 v[28:31], v[98:101], v[28:31], v[8:11]
	s_waitcnt lgkmcnt(1)
	v_mfma_f32_16x16x32_bf16 v[24:27], v[98:101], v[32:35], v[12:15]
	s_waitcnt lgkmcnt(0)
	v_mfma_f32_16x16x32_bf16 v[8:11], v[98:101], v[94:97], v[16:19]
	s_nop 0
	ds_read_b64_tr_b16 v[14:15], v59 offset:36032
	ds_read_b64_tr_b16 v[12:13], v59 offset:34944
	ds_read_b64_tr_b16 v[16:17], v59 offset:34976
	ds_read_b64_tr_b16 v[94:95], v59 offset:35008
	ds_read_b64_tr_b16 v[102:103], v59 offset:35040
	ds_read_b64_tr_b16 v[18:19], v59 offset:36064
	ds_read_b64_tr_b16 v[96:97], v59 offset:36096
	ds_read_b64_tr_b16 v[104:105], v59 offset:36128
	s_waitcnt lgkmcnt(6)
	v_mfma_f32_16x16x32_bf16 v[32:35], v[98:101], v[12:15], v[82:85]
	v_lshlrev_b64 v[12:13], 11, v[6:7]
	v_lshl_add_u64 v[110:111], v[48:49], 0, v[12:13]
	s_waitcnt lgkmcnt(2)
	v_mfma_f32_16x16x32_bf16 v[4:7], v[98:101], v[16:19], v[2:5]
	s_nop 2
	v_lshl_add_u64 v[2:3], v[46:47], 0, v[12:13]
	s_waitcnt lgkmcnt(1)
	v_mfma_f32_16x16x32_bf16 v[12:15], v[98:101], v[94:97], v[20:23]
	ds_read_b32 v50, v0 offset:4
	v_add_u32_e32 v0, s42, v69
	s_waitcnt lgkmcnt(1)
	v_mfma_f32_16x16x32_bf16 v[16:19], v[98:101], v[102:105], v[86:89]
	s_nop 2
	s_waitcnt lgkmcnt(0)
	s_barrier
	ds_read_b32 v0, v0
	v_mfma_f32_16x16x32_bf16 v[20:23], v[98:101], v[90:93], v[78:81]
	s_waitcnt vmcnt(4)
	v_mov_b64_e32 v[82:83], v[216:217]
	v_mov_b64_e32 v[84:85], v[218:219]
	v_mov_b64_e32 v[106:107], v[220:221]
	v_mov_b64_e32 v[108:109], v[222:223]
	v_mov_b64_e32 v[94:95], v[224:225]
	v_mov_b64_e32 v[96:97], v[226:227]
	v_mov_b64_e32 v[86:87], v[228:229]
	v_mov_b64_e32 v[88:89], v[230:231]
	ds_write_b128 v53, v[106:109] offset:17408
	ds_write_b128 v53, v[82:85] offset:17424
	v_lshlrev_b32_e32 v2, 16, v94
	v_and_b32_e32 v3, 0xffff0000, v94
	s_waitcnt lgkmcnt(2)
	v_pk_mul_f32 v[2:3], v[0:1], v[2:3] op_sel_hi:[0,1]
	v_cvt_pk_bf16_f32 v78, v2, v3
	v_lshlrev_b32_e32 v2, 16, v95
	v_and_b32_e32 v3, 0xffff0000, v95
	v_pk_mul_f32 v[2:3], v[0:1], v[2:3] op_sel_hi:[0,1]
	v_cvt_pk_bf16_f32 v79, v2, v3
	v_lshlrev_b32_e32 v2, 16, v96
	v_and_b32_e32 v3, 0xffff0000, v96
	v_pk_mul_f32 v[2:3], v[0:1], v[2:3] op_sel_hi:[0,1]
	v_cvt_pk_bf16_f32 v80, v2, v3
	v_lshlrev_b32_e32 v2, 16, v97
	v_and_b32_e32 v3, 0xffff0000, v97
	v_pk_mul_f32 v[2:3], v[0:1], v[2:3] op_sel_hi:[0,1]
	v_cvt_pk_bf16_f32 v81, v2, v3
	v_lshlrev_b32_e32 v2, 16, v86
	v_and_b32_e32 v3, 0xffff0000, v86
	v_pk_mul_f32 v[2:3], v[0:1], v[2:3] op_sel_hi:[0,1]
	v_cvt_pk_bf16_f32 v82, v2, v3
	v_lshlrev_b32_e32 v2, 16, v87
	v_and_b32_e32 v3, 0xffff0000, v87
	v_pk_mul_f32 v[2:3], v[0:1], v[2:3] op_sel_hi:[0,1]
	v_cvt_pk_bf16_f32 v83, v2, v3
	v_lshlrev_b32_e32 v2, 16, v88
	v_and_b32_e32 v3, 0xffff0000, v88
	v_pk_mul_f32 v[2:3], v[0:1], v[2:3] op_sel_hi:[0,1]
	v_cvt_pk_bf16_f32 v84, v2, v3
	v_lshlrev_b32_e32 v2, 16, v89
	v_and_b32_e32 v3, 0xffff0000, v89
	v_pk_mul_f32 v[2:3], v[0:1], v[2:3] op_sel_hi:[0,1]
	v_cvt_pk_bf16_f32 v85, v2, v3
	ds_write_b128 v53, v[78:81] offset:34816
	ds_write_b128 v53, v[82:85] offset:34832
	s_and_saveexec_b64 s[0:1], s[8:9]
	s_cbranch_execz .LBB0_278
	v_bfe_u32 v2, v0, 16, 1
	v_add3_u32 v0, v0, v2, s28
	v_lshrrev_b32_e32 v0, 16, v0
	v_mov_b32_e32 v2, v1
	v_mov_b32_e32 v3, v1
	ds_write_b128 v66, v[0:3] offset:52224
	ds_write_b128 v66, v[74:77] offset:52240
; template <bool OUT, bool PASS2>
; __device__ __forceinline__ void ml_block(const Args& a, unsigned char* lds_g, int rowbase, int h, int dir, f32x4 (&st)[9], int tid) {
;     ...
;         {
;             const int t = st_t, pc = st_pc;
;             const float e = eu[64 * c + t];
;             *(v4u*)(Ki + t * ML_STRIDE + 16 * pc) = k0; *(v4u*)(Ki + t * ML_STRIDE + 16 * pc + 8) = k1;
;             if (OUT) { *(v4u*)(Qi + t * ML_STRIDE + 16 * pc) = q0; *(v4u*)(Qi + t * ML_STRIDE + 16 * pc + 8) = q1; }
;             const unsigned vv[8] = {v0.x, v0.y, v0.z, v0.w, v1.x, v1.y, v1.z, v1.w}; unsigned o[8];
; #pragma unroll
;             for (int i = 0; i < 8; ++i) o[i] = pk2(bflo(vv[i]) * e, bfhi(vv[i]) * e);
;             *(v4u*)(Vi + t * ML_STRIDE + 16 * pc) = (v4u){o[0], o[1], o[2], o[3]}; *(v4u*)(Vi + t * ML_STRIDE + 16 * pc + 8) = (v4u){o[4], o[5], o[6], o[7]};
;             if (pc == 0) { *(v4u*)(AUGi + t * 16) = (v4u){f2bf(e), 0u, 0u, 0u}; *(v4u*)(AUGi + t * 16 + 8) = (v4u){0u, 0u, 0u, 0u}; }
;         }
;         WG_BAR();
;         if (ci < 3) ML_LOADC(dir ? 2 - ci : ci + 1);
;         f32x4 X[5]; float hval[4][4];
;         if (OUT) {
;             bf16x8_t qf[4];
; #pragma unroll
;             for (int ks = 0; ks < 4; ++ks) qf[ks] = frag_row(Qi, 16 * ti, 32 * ks, fr, fq);
;             bf16x8_t P[2]; bool pv[2];
; #pragma unroll
;             for (int pp = 0; pp < 2; ++pp) {
;                 f32x4 d[2];
; #pragma unroll
;                 for (int hh = 0; hh < 2; ++hh) { const int si = 2 * pp + hh; d[hh] = (f32x4){0.f, 0.f, 0.f, 0.f};
;                     const bool valid = dir ? (si >= ti) : (si <= ti);
;                     if (valid) {
; #pragma unroll
;                         for (int ks = 0; ks < 4; ++ks) d[hh] = __builtin_amdgcn_mfma_f32_16x16x32_bf16(frag_row(Ki, 16 * si, 32 * ks, fr, fq), qf[ks], d[hh], 0, 0, 0);
;                         if (si == ti) {
; #pragma unroll
;                             for (int r = 0; r < 4; ++r) { const bool keep = dir ? (4 * fq + r >= fr) : (4 * fq + r <= fr); d[hh][r] = keep ? d[hh][r] : 0.f; } } } }
;                 pv[pp] = dir ? (2 * pp + 1 >= ti) : (2 * pp <= ti);
;                 const unsigned p0 = pk2(d[0][0], d[0][1]), p1 = pk2(d[0][2], d[0][3]), p2 = pk2(d[1][0], d[1][1]), p3 = pk2(d[1][2], d[1][3]);
;                 P[pp] = __builtin_bit_cast(bf16x8_t, (v4u){p0, p1, p2, p3});
;             }
.LBB0_278:
	s_or_b64 exec, exec, s[0:1]
	s_waitcnt lgkmcnt(0)
	s_barrier
	ds_read_b64_tr_b16 v[78:79], v71 offset:17408
	ds_read_b64_tr_b16 v[80:81], v71 offset:18496
	ds_read_b64_tr_b16 v[82:83], v56 offset:34816
	ds_read_b64_tr_b16 v[86:87], v56 offset:34848
	ds_read_b64_tr_b16 v[90:91], v56 offset:34880
	ds_read_b64_tr_b16 v[94:95], v56 offset:34912
	ds_read_b64_tr_b16 v[84:85], v56 offset:35904
	ds_read_b64_tr_b16 v[88:89], v56 offset:35936
	ds_read_b64_tr_b16 v[92:93], v56 offset:35968
	ds_read_b64_tr_b16 v[96:97], v56 offset:36000
	ds_read_b64_tr_b16 v[98:99], v72 offset:17408
	ds_read_b64_tr_b16 v[100:101], v72 offset:18496
	v_pk_mul_f32 v[38:39], v[38:39], v[50:51] op_sel_hi:[1,0]
	v_pk_mul_f32 v[36:37], v[36:37], v[50:51] op_sel_hi:[1,0]
	v_pk_mul_f32 v[30:31], v[30:31], v[50:51] op_sel_hi:[1,0]
	v_pk_mul_f32 v[28:29], v[28:29], v[50:51] op_sel_hi:[1,0]
	v_pk_mul_f32 v[26:27], v[26:27], v[50:51] op_sel_hi:[1,0]
	v_pk_mul_f32 v[24:25], v[24:25], v[50:51] op_sel_hi:[1,0]
	v_pk_mul_f32 v[10:11], v[10:11], v[50:51] op_sel_hi:[1,0]
	v_pk_mul_f32 v[8:9], v[8:9], v[50:51] op_sel_hi:[1,0]
	s_waitcnt lgkmcnt(5)
	v_mfma_f32_16x16x32_bf16 v[36:39], v[78:81], v[82:85], v[36:39]
	v_mul_f32_e64 v34, v34, v50
	v_mul_f32_e64 v35, v35, v50
	v_pk_mul_f32 v[32:33], v[32:33], v[50:51] op_sel_hi:[1,0]
	v_pk_mul_f32 v[6:7], v[6:7], v[50:51] op_sel_hi:[1,0]
	s_waitcnt lgkmcnt(4)
	v_mfma_f32_16x16x32_bf16 v[28:31], v[78:81], v[86:89], v[28:31]
	v_mul_f32_e64 v4, v4, v50
	v_mul_f32_e64 v5, v5, v50
	v_pk_mul_f32 v[14:15], v[14:15], v[50:51] op_sel_hi:[1,0]
	v_pk_mul_f32 v[12:13], v[12:13], v[50:51] op_sel_hi:[1,0]
	s_waitcnt lgkmcnt(3)
	v_mfma_f32_16x16x32_bf16 v[24:27], v[78:81], v[90:93], v[24:27]
	v_mul_f32_e64 v18, v18, v50
	v_mul_f32_e64 v19, v19, v50
	v_pk_mul_f32 v[16:17], v[16:17], v[50:51] op_sel_hi:[1,0]
	v_pk_mul_f32 v[22:23], v[22:23], v[50:51] op_sel_hi:[1,0]
	s_waitcnt lgkmcnt(2)
	v_mfma_f32_16x16x32_bf16 v[8:11], v[78:81], v[94:97], v[8:11]
	ds_read_b64_tr_b16 v[84:85], v56 offset:36032
	ds_read_b64_tr_b16 v[82:83], v56 offset:34944
	ds_read_b64_tr_b16 v[86:87], v56 offset:34976
	ds_read_b64_tr_b16 v[90:91], v56 offset:35008
	ds_read_b64_tr_b16 v[94:95], v56 offset:35040
	ds_read_b64_tr_b16 v[88:89], v56 offset:36064
	ds_read_b64_tr_b16 v[92:93], v56 offset:36096
	ds_read_b64_tr_b16 v[96:97], v56 offset:36128
	v_pk_mul_f32 v[20:21], v[20:21], v[50:51] op_sel_hi:[1,0]
	v_mov_b32_e32 v0, s44
	s_waitcnt lgkmcnt(6)
	v_mfma_f32_16x16x32_bf16 v[32:35], v[78:81], v[82:85], v[32:35]
	ds_read_b64_tr_b16 v[82:83], v70 offset:52224
	ds_read_b64_tr_b16 v[84:85], v70 offset:52352
	s_waitcnt lgkmcnt(4)
	v_mfma_f32_16x16x32_bf16 v[2:5], v[78:81], v[86:89], v[4:7]
	ds_read_b64_tr_b16 v[86:87], v67 offset:52224
	ds_read_b64_tr_b16 v[88:89], v67 offset:52352
	s_nop 0
	v_or_b32_e32 v6, s43, v73
	s_waitcnt lgkmcnt(5)
	v_mfma_f32_16x16x32_bf16 v[12:15], v[78:81], v[90:93], v[12:15]
	v_ashrrev_i32_e32 v7, 31, v6
	s_waitcnt lgkmcnt(4)
	v_mfma_f32_16x16x32_bf16 v[16:19], v[78:81], v[94:97], v[16:19]
	s_waitcnt lgkmcnt(2)
	v_mfma_f32_16x16x32_bf16 v[20:23], v[78:81], v[82:85], v[20:23]
	ds_read_b64_tr_b16 v[80:81], v59 offset:35904
	ds_read_b64_tr_b16 v[78:79], v59 offset:34816
	ds_read_b64_tr_b16 v[82:83], v59 offset:34848
	ds_read_b64_tr_b16 v[90:91], v59 offset:34880
	ds_read_b64_tr_b16 v[94:95], v59 offset:34912
	ds_read_b64_tr_b16 v[84:85], v59 offset:35936
	ds_read_b64_tr_b16 v[92:93], v59 offset:35968
	ds_read_b64_tr_b16 v[96:97], v59 offset:36000
	s_waitcnt lgkmcnt(6)
	v_mfma_f32_16x16x32_bf16 v[36:39], v[98:101], v[78:81], v[36:39]
	s_waitcnt lgkmcnt(2)
	v_mfma_f32_16x16x32_bf16 v[28:31], v[98:101], v[82:85], v[28:31]
	s_waitcnt lgkmcnt(1)
	v_mfma_f32_16x16x32_bf16 v[24:27], v[98:101], v[90:93], v[24:27]
	s_waitcnt lgkmcnt(0)
	v_mfma_f32_16x16x32_bf16 v[8:11], v[98:101], v[94:97], v[8:11]
	ds_read_b64_tr_b16 v[80:81], v59 offset:36032
	ds_read_b64_tr_b16 v[78:79], v59 offset:34944
	ds_read_b64_tr_b16 v[82:83], v59 offset:34976
	ds_read_b64_tr_b16 v[90:91], v59 offset:35008
	ds_read_b64_tr_b16 v[94:95], v59 offset:35040
	ds_read_b64_tr_b16 v[84:85], v59 offset:36064
	ds_read_b64_tr_b16 v[92:93], v59 offset:36096
	ds_read_b64_tr_b16 v[96:97], v59 offset:36128
	s_waitcnt lgkmcnt(6)
	v_mfma_f32_16x16x32_bf16 v[32:35], v[98:101], v[78:81], v[32:35]
	v_lshlrev_b64 v[78:79], 11, v[6:7]
	v_lshl_add_u64 v[102:103], v[48:49], 0, v[78:79]
	s_waitcnt lgkmcnt(2)
	v_mfma_f32_16x16x32_bf16 v[4:7], v[98:101], v[82:85], v[2:5]
	s_nop 2
	v_lshl_add_u64 v[2:3], v[46:47], 0, v[78:79]
	s_waitcnt lgkmcnt(1)
	v_mfma_f32_16x16x32_bf16 v[12:15], v[98:101], v[90:93], v[12:15]
	ds_read_b32 v50, v0 offset:8
	v_add_u32_e32 v0, s45, v69
	s_waitcnt lgkmcnt(1)
	v_mfma_f32_16x16x32_bf16 v[16:19], v[98:101], v[94:97], v[16:19]
	s_waitcnt lgkmcnt(0)
	s_barrier
	ds_read_b32 v0, v0
	v_mfma_f32_16x16x32_bf16 v[20:23], v[98:101], v[86:89], v[20:23]
	s_waitcnt vmcnt(0)
	v_mov_b64_e32 v[78:79], v[232:233]
	v_mov_b64_e32 v[80:81], v[234:235]
	v_mov_b64_e32 v[82:83], v[236:237]
	v_mov_b64_e32 v[84:85], v[238:239]
	v_mov_b64_e32 v[90:91], v[240:241]
	v_mov_b64_e32 v[92:93], v[242:243]
	v_mov_b64_e32 v[94:95], v[244:245]
	v_mov_b64_e32 v[96:97], v[246:247]
	ds_write_b128 v53, v[82:85] offset:17408
	ds_write_b128 v53, v[78:81] offset:17424
	v_lshlrev_b32_e32 v2, 16, v90
	v_and_b32_e32 v3, 0xffff0000, v90
	s_waitcnt lgkmcnt(2)
	v_pk_mul_f32 v[2:3], v[0:1], v[2:3] op_sel_hi:[0,1]
	v_cvt_pk_bf16_f32 v78, v2, v3
	v_lshlrev_b32_e32 v2, 16, v91
	v_and_b32_e32 v3, 0xffff0000, v91
	v_pk_mul_f32 v[2:3], v[0:1], v[2:3] op_sel_hi:[0,1]
	v_cvt_pk_bf16_f32 v79, v2, v3
	v_lshlrev_b32_e32 v2, 16, v92
	v_and_b32_e32 v3, 0xffff0000, v92
	v_pk_mul_f32 v[2:3], v[0:1], v[2:3] op_sel_hi:[0,1]
	v_cvt_pk_bf16_f32 v80, v2, v3
	v_lshlrev_b32_e32 v2, 16, v93
	v_and_b32_e32 v3, 0xffff0000, v93
	v_pk_mul_f32 v[2:3], v[0:1], v[2:3] op_sel_hi:[0,1]
	v_cvt_pk_bf16_f32 v81, v2, v3
	v_lshlrev_b32_e32 v2, 16, v94
	v_and_b32_e32 v3, 0xffff0000, v94
	v_pk_mul_f32 v[2:3], v[0:1], v[2:3] op_sel_hi:[0,1]
	v_cvt_pk_bf16_f32 v82, v2, v3
	v_lshlrev_b32_e32 v2, 16, v95
	v_and_b32_e32 v3, 0xffff0000, v95
	v_pk_mul_f32 v[2:3], v[0:1], v[2:3] op_sel_hi:[0,1]
	v_cvt_pk_bf16_f32 v83, v2, v3
	v_lshlrev_b32_e32 v2, 16, v96
	v_and_b32_e32 v3, 0xffff0000, v96
	v_pk_mul_f32 v[2:3], v[0:1], v[2:3] op_sel_hi:[0,1]
	v_cvt_pk_bf16_f32 v84, v2, v3
	v_lshlrev_b32_e32 v2, 16, v97
	v_and_b32_e32 v3, 0xffff0000, v97
	v_pk_mul_f32 v[2:3], v[0:1], v[2:3] op_sel_hi:[0,1]
	v_cvt_pk_bf16_f32 v85, v2, v3
	ds_write_b128 v53, v[78:81] offset:34816
	ds_write_b128 v53, v[82:85] offset:34832
	s_and_saveexec_b64 s[0:1], s[8:9]
	s_cbranch_execz .LBB0_280
	v_bfe_u32 v2, v0, 16, 1
	v_add3_u32 v0, v0, v2, s28
	v_lshrrev_b32_e32 v0, 16, v0
	v_mov_b32_e32 v2, v1
	v_mov_b32_e32 v3, v1
	ds_write_b128 v66, v[0:3] offset:52224
	ds_write_b128 v66, v[74:77] offset:52240

; __device__ __forceinline__ void phase3(const Args& a, unsigned char* lds_g, int tid) {
;     ...
;         int q0 = (int)blockIdx.x, qstep = (int)gridDim.x;
;         if (gridDim.x == 256) q0 = blockIdx.x >= 128 ? (int)blockIdx.x - 128 : 128;
;         for (int qu = q0; qu < 128; qu += qstep) ml_state_quad(a, lds_g, qu, tid);
;     }
;     bf16x8_t wl[2][2][4]; int wl_blk = -1;
;     for (int u = blockIdx.x; u < 4 * 36 * 8; u += gridDim.x) { const int blk = u & 7, q = u >> 3; lru_unit<false>(a, lds_g, q / 36, q % 36, blk, tid, wl, wl_blk); }
.LBB0_282:
	s_cmpk_gt_i32 s83, 0x47f
	s_cbranch_scc1 .LBB0_315
	s_add_u32 s14, s84, 0x21000000
	s_addc_u32 s15, s85, 0
	s_add_u32 s48, s84, 0x500000
	s_addc_u32 s49, s85, 0
	s_add_u32 s2, s84, 0x3d200000
	s_addc_u32 s3, s85, 0
	v_mbcnt_lo_u32_b32 v0, -1, 0
	s_add_u32 s47, s84, 0x4800000
	v_mbcnt_hi_u32_b32 v185, -1, v0
	v_mov_b32_e32 v0, 0x80
	s_addc_u32 s64, s85, 0
	s_mov_b32 s42, -1
	v_mov_b32_e32 v129, 0
	s_movk_i32 s65, 0x1000
	s_movk_i32 s68, 0x100
	s_mov_b64 s[50:51], 0x1000
	s_mov_b64 s[54:55], 0x2000
	s_movk_i32 s69, 0x2000
	s_mov_b64 s[56:57], 0x3000
	s_movk_i32 s72, 0x3000
	s_movk_i32 s33, 0x210
	s_movk_i32 s34, 0x110
	s_mov_b32 s35, 0xc1a00000
	s_mov_b32 s36, 0x3f2aaaab
	v_mov_b32_e32 v181, 0x3ecc95a3
	s_mov_b32 s37, 0x3f317218
	s_mov_b32 s38, 0x7f800000
	s_mov_b32 s39, 0x33800000
	s_movk_i32 s40, 0x840
	v_mov_b32_e32 v130, 0x3f317218
	v_mov_b32_e32 v182, 0x7f800000
	v_mov_b32_e32 v183, 0x7fc00000
	v_mov_b32_e32 v184, 0xff800000
	v_mov_b32_e32 v186, 0xc0
	v_lshl_or_b32 v187, v185, 2, v0
	s_mov_b32 s101, s82
	s_movk_i32 s100, 0x480
	s_mov_b32 s41, s83
	s_cmpk_lg_i32 s82, 0x100
	s_cbranch_scc1 .Lp2_plain
	s_movk_i32 s101, 0x80
	s_add_i32 s41, s83, 0x280
	s_cmpk_lt_i32 s83, 0x80
	s_cselect_b32 s41, s83, s41
	s_cselect_b32 s100, 0x300, s100
